# prologue/epilogue de-serialisation: the six per-unit branch-gate loads are issued early and together (two before the selection-mask exchange, four after the selected branch) instead of load-wait-use o
# speedup vs baseline: 1.0054x; 1.0054x over previous
; __device__ __forceinline__ unsigned pk2(float lo, float hi) { const f32x2 v = {lo, hi}; return __builtin_bit_cast(unsigned, __builtin_convertvector(v, nbf16x2)); }
; __device__ __forceinline__ void nsa_unit(unsigned char* ws, LAS unsigned char* lds, const LAS float* lut, int b, int g, int tau, int tid_in) {
;     ...
; #pragma unroll
;         for (int c = 0; c < 2; ++c) { const float sc = NSA_GATE(c, 2) / fmaxf(st[c].l[0], 1e-30f);
;             bf16_t* yo = (bf16_t*)(ws + WS_YNSA) + ((size_t)b * SEQ + tq[c]) * 1024 + h * 64 + 4 * q;
; #pragma unroll
;             for (int dt = 0; dt < 4; ++dt) { const f32x4 rv = resw[(c * 4 + dt) * 64] + O[c][dt] * sc; u32x2 o; o.x = pk2(rv[0], rv[1]); o.y = pk2(rv[2], rv[3]); *(u32x2*)(yo + 16 * dt) = o; } }
.LBB0_1020:
	s_waitcnt vmcnt(1)
	v_lshl_add_u64 v[22:23], s[40:41], 0, v[152:153]
	v_lshl_add_u64 v[6:7], v[22:23], 0, v[168:169]
	v_mov_b32_e32 v3, v246
	s_waitcnt vmcnt(0)
	v_max_f32_e32 v28, v70, v70
	v_max_f32_e32 v28, 0xda24260, v28
	v_lshlrev_b32_e32 v152, 1, v174
	v_lshl_add_u64 v[26:27], s[42:43], 0, v[152:153]
	v_lshlrev_b32_e32 v152, 1, v183
	v_lshlrev_b64 v[24:25], 11, v[158:159]
	v_lshl_add_u64 v[26:27], v[26:27], 0, v[152:153]
	v_lshl_add_u64 v[24:25], v[26:27], 0, v[24:25]
	v_lshl_add_u64 v[22:23], v[22:23], 0, v[166:167]
	s_add_i32 s81, s81, 1
	s_add_i32 s80, s80, 2
	s_cmp_eq_u32 s81, 16
	s_mov_b32 s84, s86
	s_waitcnt vmcnt(0)
	v_div_scale_f32 v29, s[2:3], v28, v28, v3
	v_rcp_f32_e32 v30, v29
	v_div_scale_f32 v31, vcc, v3, v28, v3
	v_fma_f32 v32, -v29, v30, 1.0
	v_fmac_f32_e32 v30, v32, v30
	v_mul_f32_e32 v32, v31, v30
	v_fma_f32 v33, -v29, v32, v31
	v_fmac_f32_e32 v32, v33, v30
	v_fma_f32 v29, -v29, v32, v31
	v_div_fmas_f32 v29, v29, v30, v32
	v_div_fixup_f32 v28, v29, v28, v3
	s_waitcnt lgkmcnt(3)
	v_pk_fma_f32 v[8:9], v[84:85], v[28:29], v[212:213] op_sel_hi:[1,0,1]
	v_pk_fma_f32 v[6:7], v[82:83], v[28:29], v[210:211] op_sel_hi:[1,0,1]
	s_waitcnt lgkmcnt(2)
	v_pk_fma_f32 v[12:13], v[104:105], v[28:29], v[216:217] op_sel_hi:[1,0,1]
	v_pk_fma_f32 v[10:11], v[102:103], v[28:29], v[214:215] op_sel_hi:[1,0,1]
	s_waitcnt lgkmcnt(1)
	v_pk_fma_f32 v[16:17], v[108:109], v[28:29], v[220:221] op_sel_hi:[1,0,1]
	v_pk_fma_f32 v[14:15], v[106:107], v[28:29], v[218:219] op_sel_hi:[1,0,1]
	s_waitcnt lgkmcnt(0)
	v_pk_fma_f32 v[20:21], v[116:117], v[28:29], v[224:225] op_sel_hi:[1,0,1]
	v_pk_fma_f32 v[18:19], v[114:115], v[28:29], v[222:223] op_sel_hi:[1,0,1]
	v_cvt_pk_bf16_f32 v6, v6, v7
	v_cvt_pk_bf16_f32 v7, v8, v9
	v_cvt_pk_bf16_f32 v8, v10, v11
	v_cvt_pk_bf16_f32 v9, v12, v13
	v_cvt_pk_bf16_f32 v10, v14, v15
	v_cvt_pk_bf16_f32 v11, v16, v17
	v_cvt_pk_bf16_f32 v12, v18, v19
	v_cvt_pk_bf16_f32 v13, v20, v21
	global_store_dwordx2 v[24:25], v[6:7], off
	global_store_dwordx2 v[24:25], v[8:9], off offset:32
	global_store_dwordx2 v[24:25], v[10:11], off offset:64
	global_store_dwordx2 v[24:25], v[12:13], off offset:96
	v_mov_b32_e32 v3, v248
	v_max_f32_e32 v22, v74, v74
	v_lshlrev_b64 v[20:21], 11, v[4:5]
	v_max_f32_e32 v1, 0xda24260, v22
	v_lshl_add_u64 v[20:21], v[26:27], 0, v[20:21]
	v_div_scale_f32 v22, s[2:3], v1, v1, v3
	v_rcp_f32_e32 v23, v22
	v_div_scale_f32 v24, vcc, v3, v1, v3
	v_fma_f32 v25, -v22, v23, 1.0
	v_fmac_f32_e32 v23, v25, v23
	v_mul_f32_e32 v25, v24, v23
	v_fma_f32 v26, -v22, v25, v24
	v_fmac_f32_e32 v25, v26, v23
	v_fma_f32 v22, -v22, v25, v24
	v_div_fmas_f32 v22, v22, v23, v25
	v_div_fixup_f32 v22, v22, v1, v3
	s_waitcnt lgkmcnt(3)
	v_pk_fma_f32 v[6:7], v[80:81], v[22:23], v[228:229] op_sel_hi:[1,0,1]
	v_pk_fma_f32 v[4:5], v[78:79], v[22:23], v[226:227] op_sel_hi:[1,0,1]
	s_waitcnt lgkmcnt(2)
	v_pk_fma_f32 v[10:11], v[96:97], v[22:23], v[232:233] op_sel_hi:[1,0,1]
	v_pk_fma_f32 v[8:9], v[94:95], v[22:23], v[230:231] op_sel_hi:[1,0,1]
	s_waitcnt lgkmcnt(1)
	v_pk_fma_f32 v[14:15], v[100:101], v[22:23], v[236:237] op_sel_hi:[1,0,1]
	v_pk_fma_f32 v[12:13], v[98:99], v[22:23], v[234:235] op_sel_hi:[1,0,1]
	s_waitcnt lgkmcnt(0)
	v_pk_fma_f32 v[18:19], v[112:113], v[22:23], v[240:241] op_sel_hi:[1,0,1]
	v_pk_fma_f32 v[16:17], v[110:111], v[22:23], v[238:239] op_sel_hi:[1,0,1]
	v_cvt_pk_bf16_f32 v4, v4, v5
	v_cvt_pk_bf16_f32 v5, v6, v7
	v_cvt_pk_bf16_f32 v6, v8, v9
	v_cvt_pk_bf16_f32 v7, v10, v11
	v_cvt_pk_bf16_f32 v8, v12, v13
	v_cvt_pk_bf16_f32 v9, v14, v15
	v_cvt_pk_bf16_f32 v10, v16, v17
	v_cvt_pk_bf16_f32 v11, v18, v19
	global_store_dwordx2 v[20:21], v[4:5], off
	global_store_dwordx2 v[20:21], v[6:7], off offset:32
	global_store_dwordx2 v[20:21], v[8:9], off offset:64
	global_store_dwordx2 v[20:21], v[10:11], off offset:96
	s_cbranch_scc1 .LBB0_1348

; #define LAS __attribute__((address_space(3)))
; __device__ __forceinline__ unsigned or_x16(unsigned u) { return u | __shfl_xor(u, 16); }
; __device__ __forceinline__ unsigned or_x32(unsigned u) { return u | __shfl_xor(u, 32); }
; __device__ __forceinline__ void select_blocks8(const LAS float* impw, LAS unsigned* mk, int lane, int cur, unsigned (&u)[2][4]) {
;     ...
; #pragma unroll
;     for (int c = 0; c < 2; ++c) {
;         if (i == 0) *(LAS u32x4*)(mk + (4 * c + k) * 4) = (u32x4){m4[c][0], m4[c][1], m4[c][2], m4[c][3]};
; #pragma unroll
;         for (int x = 0; x < 4; ++x) { unsigned v = m4[c][x]; v = or_x16(v); v = or_x32(v); u[c][x] = __builtin_amdgcn_readfirstlane(v); }
;     }
; __device__ __forceinline__ void nsa_unit(unsigned char* ws, LAS unsigned char* lds, const LAS float* lut, int b, int g, int tau, int tid_in) {
;     ...
;     LAS unsigned* selw = (LAS unsigned*)(lds + TILES_OFF) + wave * 32;
;     select_blocks8(impw, selw, lane, cur, u);
;     __syncthreads();
; #pragma unroll
;     for (int c = 0; c < 2; ++c) { const float gc = NSA_GATE(c, 0);
; #pragma unroll
;         for (int dt = 0; dt < 4; ++dt) resw[(c * 4 + dt) * 64] = Oc[c][dt] * gc; }
.LBB0_1173:
	s_lshl_b32 s1, s91, 7
	s_add_i32 s24, s1, 0
	s_add_i32 s24, s24, 0x22d00
	v_cmp_eq_u32_e32 vcc, 0, v187
	v_add_u32_e32 v4, s24, v1
	s_and_saveexec_b64 s[6:7], vcc
	ds_write_b128 v4, v[74:77]
	s_or_b64 exec, exec, s[6:7]
	v_and_b32_e32 v5, 64, v176
	v_xor_b32_e32 v3, 16, v176
	v_add_u32_e32 v5, 64, v5
	v_cmp_lt_i32_e64 s[6:7], v3, v5
	v_xor_b32_e32 v78, 32, v176
	s_nop 0
	v_cndmask_b32_e64 v3, v176, v3, s[6:7]
	v_cmp_lt_i32_e64 s[6:7], v78, v5
	v_lshlrev_b32_e32 v3, 2, v3
	s_nop 0
	v_cndmask_b32_e64 v5, v176, v78, s[6:7]
	v_lshlrev_b32_e32 v155, 2, v5
	ds_bpermute_b32 v5, v3, v74
	s_waitcnt lgkmcnt(0)
	v_or_b32_e32 v5, v5, v74
	ds_bpermute_b32 v74, v155, v5
	s_waitcnt lgkmcnt(0)
	v_or_b32_e32 v5, v74, v5
	s_nop 0
	v_readfirstlane_b32 s17, v5
	ds_bpermute_b32 v5, v3, v75
	s_waitcnt lgkmcnt(0)
	v_or_b32_e32 v5, v5, v75
	ds_bpermute_b32 v74, v155, v5
	s_waitcnt lgkmcnt(0)
	v_or_b32_e32 v5, v74, v5
	s_nop 0
	v_readfirstlane_b32 s38, v5
	ds_bpermute_b32 v5, v3, v76
	s_waitcnt lgkmcnt(0)
	v_or_b32_e32 v5, v5, v76
	ds_bpermute_b32 v74, v155, v5
	s_waitcnt lgkmcnt(0)
	v_or_b32_e32 v5, v74, v5
	s_nop 0
	v_readfirstlane_b32 s39, v5
	ds_bpermute_b32 v5, v3, v77
	s_waitcnt lgkmcnt(0)
	v_or_b32_e32 v5, v5, v77
	ds_bpermute_b32 v74, v155, v5
	s_waitcnt lgkmcnt(0)
	v_or_b32_e32 v5, v74, v5
	s_nop 0
	v_readfirstlane_b32 s5, v5
	s_and_saveexec_b64 s[6:7], vcc
	ds_write_b128 v4, v[70:73] offset:64
	s_or_b64 exec, exec, s[6:7]
	ds_bpermute_b32 v4, v3, v70
	s_lshl_b32 s6, s2, 13
	s_mov_b32 s7, s27
	v_lshl_add_u64 v[158:159], s[6:7], 0, v[164:165]
	v_mul_u32_u24_e32 v242, 3, v191
	v_lshlrev_b32_e32 v242, 2, v242
	v_mov_b32_e32 v243, 0
	v_lshl_add_u64 v[242:243], s[28:29], 0, v[242:243]
	v_mad_u64_u32 v[244:245], s[2:3], v158, s0, v[242:243]
	v_mad_i32_i24 v245, v159, s0, v245
	global_load_dword v254, v[244:245], off
	v_lshl_add_u64 v[248:249], s[6:7], 0, v[108:109]
	v_mad_u64_u32 v[250:251], s[2:3], v248, s0, v[242:243]
	v_mad_i32_i24 v251, v249, s0, v251
	global_load_dword v255, v[250:251], off
	s_waitcnt lgkmcnt(0)
	v_or_b32_e32 v4, v4, v70
	ds_bpermute_b32 v5, v155, v4
	s_barrier
	s_waitcnt lgkmcnt(0)
	s_lshl_b32 s1, s91, 13
	s_add_i32 s1, s1, 0
	v_or_b32_e32 v74, v5, v4
	ds_bpermute_b32 v4, v3, v71
	v_lshl_add_u32 v1, v1, 4, s1
	v_add_u32_e32 v1, 0x10000, v1
	s_movk_i32 s1, 0x70
	s_andn2_b64 vcc, exec, s[50:51]
	s_waitcnt lgkmcnt(0)
	v_or_b32_e32 v4, v4, v71
	ds_bpermute_b32 v5, v155, v4
	s_waitcnt lgkmcnt(0)
	v_or_b32_e32 v75, v5, v4
	ds_bpermute_b32 v4, v3, v72
	v_readfirstlane_b32 s73, v75
	s_waitcnt lgkmcnt(0)
	v_or_b32_e32 v4, v4, v72
	ds_bpermute_b32 v5, v155, v4
	s_waitcnt lgkmcnt(0)
	v_or_b32_e32 v72, v5, v4
	ds_bpermute_b32 v4, v3, v73
	s_waitcnt lgkmcnt(0)
	v_or_b32_e32 v4, v4, v73
	ds_bpermute_b32 v5, v155, v4
	s_waitcnt lgkmcnt(0)
	v_or_b32_e32 v73, v5, v4
	v_mul_u32_u24_e32 v4, 3, v191
	v_lshlrev_b32_e32 v152, 2, v4
	v_lshl_add_u64 v[70:71], s[28:29], 0, v[152:153]
	v_mad_u64_u32 v[4:5], s[2:3], v158, s0, v[70:71]
	v_mad_i32_i24 v5, v159, s0, v5
	v_readfirstlane_b32 s72, v73
	s_waitcnt vmcnt(0)
	v_mov_b32_e32 v4, v254
	v_pk_mul_f32 v[212:213], v[56:57], v[4:5] op_sel_hi:[1,0]
	v_pk_mul_f32 v[210:211], v[54:55], v[4:5] op_sel_hi:[1,0]
	v_pk_mul_f32 v[216:217], v[60:61], v[4:5] op_sel_hi:[1,0]
	v_pk_mul_f32 v[214:215], v[58:59], v[4:5] op_sel_hi:[1,0]
	v_pk_mul_f32 v[220:221], v[64:65], v[4:5] op_sel_hi:[1,0]
	v_pk_mul_f32 v[218:219], v[62:63], v[4:5] op_sel_hi:[1,0]
	v_pk_mul_f32 v[224:225], v[68:69], v[4:5] op_sel_hi:[1,0]
	v_pk_mul_f32 v[222:223], v[66:67], v[4:5] op_sel_hi:[1,0]
	v_lshl_add_u64 v[4:5], s[6:7], 0, v[108:109]
	v_mad_u64_u32 v[54:55], s[2:3], v4, s0, v[70:71]
	v_mad_i32_i24 v55, v5, s0, v55
	v_readfirstlane_b32 s2, v74
	v_readfirstlane_b32 s3, v72
	s_waitcnt vmcnt(0)
	v_mov_b32_e32 v54, v255
	v_pk_mul_f32 v[228:229], v[40:41], v[54:55] op_sel_hi:[1,0]
	v_pk_mul_f32 v[226:227], v[38:39], v[54:55] op_sel_hi:[1,0]
	v_pk_mul_f32 v[232:233], v[44:45], v[54:55] op_sel_hi:[1,0]
	v_pk_mul_f32 v[230:231], v[42:43], v[54:55] op_sel_hi:[1,0]
	v_pk_mul_f32 v[236:237], v[48:49], v[54:55] op_sel_hi:[1,0]
	v_pk_mul_f32 v[234:235], v[46:47], v[54:55] op_sel_hi:[1,0]
	v_pk_mul_f32 v[240:241], v[52:53], v[54:55] op_sel_hi:[1,0]
	v_pk_mul_f32 v[238:239], v[50:51], v[54:55] op_sel_hi:[1,0]
	s_mov_b32 s98, 0
	s_mov_b32 s100, -1
	s_mov_b32 s101, 0
	s_mov_b32 s99, 0
	v_and_b32_e32 v248, 3, v185
	v_lshlrev_b32_e32 v249, 2, v248
	v_lshl_add_u32 v248, v186, 6, v249
	v_add_u32_e32 v248, 0x10000, v248
	v_add_u32_e32 v249, 0x20400, v249
	v_lshlrev_b32_e32 v250, 2, v184
	v_and_b32_e32 v251, 63, v185
	v_lshlrev_b32_e32 v251, 4, v251
	v_add_u32_e32 v251, 0x22d00, v251
	ds_read_b128 v[242:245], v251
	s_waitcnt lgkmcnt(0)
	v_xor_b32_e32 v39, v110, v185
	v_lshlrev_b32_e32 v38, 7, v110
	v_lshlrev_b32_e32 v39, 4, v39
	v_and_or_b32 v38, v39, s1, v38
	v_add_u32_e32 v188, 0, v38
	v_cndmask_b32_e64 v38, 0, 1, s[50:51]
	v_cmp_ne_u32_e64 s[6:7], 1, v38
	ds_write_b128 v188, v[26:29]
	ds_write_b128 v188, v[22:25] offset:32768
	s_cbranch_vccnz .LBB0_1179
	ds_write_b128 v188, v[30:33] offset:8192
	ds_write_b128 v188, v[34:37] offset:40960

; __device__ __forceinline__ void nsa_unit(unsigned char* ws, LAS unsigned char* lds, const LAS float* lut, int b, int g, int tau, int tid_in) {
;     ...
; #pragma unroll
;         for (int c = 0; c < 2; ++c) { const float sc = NSA_GATE(c, 1) / fmaxf(st[c].l[0], 1e-30f);
; #pragma unroll
;             for (int dt = 0; dt < 4; ++dt) resw[(c * 4 + dt) * 64] = resw[(c * 4 + dt) * 64] + O[c][dt] * sc; }
;     }
;     {
;         f32x4 O[2][4]; Softmax st[2];
; #pragma unroll
;         for (int c = 0; c < 2; ++c) { st[c].m = -1e30f; st[c].l = z4;
; #pragma unroll
;             for (int dt = 0; dt < 4; ++dt) O[c][dt] = z4; }
;         const unsigned char* kg = ws + WS_KW + ((size_t)b * SEQ * 256 + g * 64) * 2;
;         const unsigned char* vg = ws + WS_VWT + ((size_t)((b * 4 + g) * 64)) * SEQ * 2;
;         const int jlo = cur >= 8 ? cur - 8 : 0;
.LBB0_1296:
	s_waitcnt vmcnt(0)
	v_lshl_add_u64 v[34:35], s[30:31], 0, v[152:153]
	v_lshl_add_u64 v[30:31], v[34:35], 0, v[168:169]
	global_load_dword v30, v[30:31], off
	v_lshl_add_u64 v[242:243], v[34:35], 0, v[166:167]
	global_load_dword v242, v[242:243], off
	v_lshl_add_u64 v[244:245], s[40:41], 0, v[152:153]
	v_lshl_add_u64 v[246:247], v[244:245], 0, v[168:169]
	v_lshl_add_u64 v[248:249], v[244:245], 0, v[166:167]
	global_load_dword v246, v[246:247], off
	global_load_dword v248, v[248:249], off
	v_max_f32_e32 v31, v74, v74
	v_max_f32_e32 v31, 0xda24260, v31
	s_add_i32 s1, s37, -3
	s_cmp_le_i32 s50, s37
	s_cselect_b64 s[8:9], -1, 0
	s_cmp_gt_i32 s50, s37
	s_waitcnt vmcnt(0)
	v_div_scale_f32 v32, s[2:3], v31, v31, v30
	v_rcp_f32_e32 v33, v32
	s_nop 0
	v_fma_f32 v36, -v32, v33, 1.0
	v_fmac_f32_e32 v33, v36, v33
	v_div_scale_f32 v36, vcc, v30, v31, v30
	v_mul_f32_e32 v37, v36, v33
	v_fma_f32 v59, -v32, v37, v36
	v_fmac_f32_e32 v37, v59, v33
	v_fma_f32 v32, -v32, v37, v36
	v_div_fmas_f32 v32, v32, v33, v37
	v_div_fixup_f32 v36, v32, v31, v30
	s_waitcnt lgkmcnt(0)
	v_pk_fma_f32 v[212:213], v[72:73], v[36:37], v[212:213] op_sel_hi:[1,0,1]
	v_pk_fma_f32 v[210:211], v[70:71], v[36:37], v[210:211] op_sel_hi:[1,0,1]
	s_waitcnt lgkmcnt(0)
	v_pk_fma_f32 v[216:217], v[68:69], v[36:37], v[216:217] op_sel_hi:[1,0,1]
	v_pk_fma_f32 v[214:215], v[66:67], v[36:37], v[214:215] op_sel_hi:[1,0,1]
	s_waitcnt lgkmcnt(0)
	v_pk_fma_f32 v[220:221], v[64:65], v[36:37], v[220:221] op_sel_hi:[1,0,1]
	v_pk_fma_f32 v[218:219], v[62:63], v[36:37], v[218:219] op_sel_hi:[1,0,1]
	s_waitcnt lgkmcnt(0)
	v_pk_fma_f32 v[224:225], v[56:57], v[36:37], v[224:225] op_sel_hi:[1,0,1]
	v_pk_fma_f32 v[222:223], v[54:55], v[36:37], v[222:223] op_sel_hi:[1,0,1]
	v_lshl_add_u64 v[30:31], v[34:35], 0, v[166:167]
	v_max_f32_e32 v31, v58, v58
	v_max_f32_e32 v31, 0xda24260, v31
	s_waitcnt vmcnt(0)
	v_mov_b32_e32 v30, v242
	v_div_scale_f32 v32, s[2:3], v31, v31, v30
	v_rcp_f32_e32 v33, v32
	s_nop 0
	v_fma_f32 v34, -v32, v33, 1.0
	v_fmac_f32_e32 v33, v34, v33
	v_div_scale_f32 v34, vcc, v30, v31, v30
	v_mul_f32_e32 v35, v34, v33
	v_fma_f32 v36, -v32, v35, v34
	v_fmac_f32_e32 v35, v36, v33
	v_fma_f32 v32, -v32, v35, v34
	v_div_fmas_f32 v32, v32, v33, v35
	v_div_fixup_f32 v34, v32, v31, v30
	s_waitcnt lgkmcnt(0)
	v_pk_fma_f32 v[228:229], v[52:53], v[34:35], v[228:229] op_sel_hi:[1,0,1]
	v_pk_fma_f32 v[226:227], v[50:51], v[34:35], v[226:227] op_sel_hi:[1,0,1]
	s_waitcnt lgkmcnt(0)
	v_pk_fma_f32 v[232:233], v[48:49], v[34:35], v[232:233] op_sel_hi:[1,0,1]
	v_pk_fma_f32 v[230:231], v[46:47], v[34:35], v[230:231] op_sel_hi:[1,0,1]
	s_waitcnt lgkmcnt(0)
	v_pk_fma_f32 v[236:237], v[44:45], v[34:35], v[236:237] op_sel_hi:[1,0,1]
	v_pk_fma_f32 v[234:235], v[42:43], v[34:35], v[234:235] op_sel_hi:[1,0,1]
	s_waitcnt lgkmcnt(0)
	v_pk_fma_f32 v[238:239], v[38:39], v[34:35], v[238:239] op_sel_hi:[1,0,1]
	v_pk_fma_f32 v[240:241], v[40:41], v[34:35], v[240:241] op_sel_hi:[1,0,1]
	ds_write_b128 v188, v[26:29]
	ds_write_b128 v188, v[22:25] offset:32768
	s_waitcnt lgkmcnt(0)
	s_barrier
	s_cbranch_scc1 .LBB0_1322
	v_and_b32_e32 v30, 7, v185
	v_bitop3_b32 v30, v186, v30, 4 bitop3:0x36
	v_lshlrev_b32_e32 v175, 4, v30
	v_add_u32_e32 v30, s92, v184
	v_sub_u32_e32 v30, v30, v183
	s_lshl_b32 s3, s16, 6
	v_subrev_u32_e32 v30, s3, v30
	v_bitop3_b32 v31, v186, v185, 7 bitop3:0x78
	v_add_u32_e32 v191, 0x204, v30
	s_lshl_b32 s3, s16, 8
	v_lshlrev_b32_e32 v30, 4, v186
	v_lshlrev_b32_e32 v173, 4, v31
	v_add3_u32 v30, v190, s3, v30
	v_add_lshl_u32 v31, v184, v189, 2
	v_sub_u32_e32 v30, v30, v31
	s_lshl_b32 s3, s91, 5
	v_subrev_u32_e32 v30, s3, v30
	s_lshl_b32 s3, s37, 8
	v_subrev_u32_e32 v30, s3, v30
	v_readlane_b32 s3, v253, 56
	s_mov_b32 s17, s27
	s_add_i32 s2, s16, -6
	v_add_u32_e32 v192, s3, v30
	s_lshl_b64 s[6:7], s[16:17], 15
	v_readlane_b32 s3, v253, 49
	s_add_u32 s3, s3, s6
	v_readlane_b32 s5, v253, 50
	s_addc_u32 s5, s5, s7
	s_add_u32 s6, s3, s55
	v_lshl_add_u64 v[30:31], v[160:161], 0, v[156:157]
	s_addc_u32 s7, s5, s93
	v_lshl_add_u64 v[164:165], s[6:7], 0, v[30:31]
	s_lshl_b64 s[6:7], s[16:17], 7
	v_readlane_b32 s3, v253, 51
	v_lshl_add_u64 v[30:31], v[160:161], 0, s[18:19]
	s_add_u32 s6, s3, s6
	v_readlane_b32 s3, v253, 53
	v_lshl_add_u64 v[30:31], v[30:31], 0, v[162:163]
	s_addc_u32 s7, s3, s7
	v_mov_b32_e32 v32, v153
	v_mov_b32_e32 v33, v153
	v_lshl_add_u64 v[170:171], s[6:7], 0, v[30:31]
	v_mov_b32_e32 v30, v153
	v_mov_b32_e32 v31, v153
	v_mov_b64_e32 v[40:41], v[32:33]
	v_mov_b64_e32 v[44:45], v[32:33]
	v_mov_b64_e32 v[56:57], v[32:33]
	v_mov_b64_e32 v[36:37], v[32:33]
	v_mov_b64_e32 v[48:49], v[32:33]
	v_mov_b64_e32 v[52:53], v[32:33]
	v_mov_b64_e32 v[60:61], v[32:33]
	v_mov_b64_e32 v[64:65], v[32:33]
	v_mov_b64_e32 v[68:69], v[32:33]
	v_lshlrev_b32_e32 v172, 7, v187
	v_mov_b32_e32 v193, 0xf149f2ca
	s_mov_b32 s3, 0xffff0000
	s_mov_b32 s5, s16
	v_mov_b64_e32 v[38:39], v[30:31]
	v_mov_b64_e32 v[42:43], v[30:31]
	v_mov_b64_e32 v[54:55], v[30:31]
	v_mov_b64_e32 v[34:35], v[30:31]
	v_mov_b64_e32 v[46:47], v[30:31]
	v_mov_b64_e32 v[50:51], v[30:31]
	v_mov_b64_e32 v[58:59], v[30:31]
	v_mov_b64_e32 v[62:63], v[30:31]
	v_mov_b64_e32 v[66:67], v[30:31]
	v_mov_b32_e32 v197, 0xf149f2ca
